# prologue: experts 0-2 + w_in0 + x only; beside first GEMM (64 WGs): experts 3-4 + the seven later-used dense weight matrices; recurrence phase: experts 5-7; early GEMM barrier
# speedup vs baseline: 1.0214x; 1.0027x over previous
.LBB0_15:
	v_lshlrev_b32_e32 v67, 2, v0
	v_and_b32_e32 v71, 60, v67
	v_bfe_u32 v93, v0, 4, 2
	v_lshlrev_b32_e32 v1, 2, v71
	v_mul_u32_u24_e32 v2, 0x104, v93
	v_add3_u32 v73, v31, v1, v2
	v_lshlrev_b32_e32 v1, 3, v0
	v_and_b32_e32 v2, 56, v1
	v_mul_u32_u24_e32 v3, 0x104, v2
	v_lshlrev_b32_e32 v4, 2, v66
	s_movk_i32 s0, 0x400
	v_mov_b32_e32 v77, 0
	v_add3_u32 v88, v31, v3, v4
	v_or_b32_e32 v89, 32, v66
	v_or_b32_e32 v90, 40, v66
	v_or_b32_e32 v91, 48, v66
	v_or_b32_e32 v92, 56, v66
	v_cmp_gt_i32_e64 s[6:7], s0, v69
	v_lshlrev_b32_e32 v76, 1, v2
	v_lshlrev_b32_e32 v94, 6, v186
	s_cmp_eq_u32 s99, 0
	s_cbranch_scc1 .LBB0_226
	s_and_saveexec_b64 s[0:1], s[6:7]
	s_cbranch_execz .LBB0_50
	v_lshl_add_u64 v[2:3], s[58:59], 0, v[76:77]
	s_mov_b64 s[8:9], 0x3da00000
	v_lshl_add_u64 v[82:83], v[2:3], 0, s[8:9]
	v_lshl_or_b32 v77, s96, 9, v94
	s_lshl_b32 s14, s3, 6
	s_mov_b64 s[8:9], 0
	s_movk_i32 s15, 0x800
	s_movk_i32 s16, 0x3ff
	v_mov_b32_e32 v95, v69
	s_branch .LBB0_18

.LBB0_226:
	s_or_b64 exec, exec, s[0:1]
	s_cmp_eq_u32 s99, 0
	s_cbranch_scc0 .Lconv_ret_h0
	s_movk_i32 s0, 0xc00
	v_cmp_gt_i32_e32 vcc, s0, v69
	s_and_saveexec_b64 s[0:1], vcc
	s_cbranch_execz .LBB0_261
	v_mov_b32_e32 v77, 0
	v_lshl_add_u64 v[2:3], s[58:59], 0, v[76:77]
	s_mov_b64 s[6:7], 0x36100000
	v_lshl_or_b32 v77, s96, 9, v94
	v_lshl_add_u64 v[74:75], v[2:3], 0, s[6:7]
	v_or_b32_e32 v2, v77, v93
	s_movk_i32 s15, 0x1800
	s_lshl_b32 s14, s3, 6
	v_mul_lo_u32 v76, v2, s15
	s_mul_i32 s16, s3, 0x60000
	s_mov_b64 s[8:9], 0
	s_mov_b32 s17, 0xff400000
	s_movk_i32 s18, 0xbff
	s_branch .LBB0_229

.LBB0_400:
	s_cmp_lt_i32 s76, 2
	s_cselect_b64 s[6:7], -1, 0
	s_add_u32 s82, s58, 0x32100000
	s_addc_u32 s83, s59, 0
	s_and_b64 s[0:1], s[6:7], s[0:1]
	s_andn2_b64 vcc, exec, s[0:1]
	s_cbranch_vccnz .LBB0_417
	s_mov_b32 s101, s2
	s_cmpk_lt_i32 s96, 192
	s_cbranch_scc1 .Lh0_gemm
	s_sub_i32 s96, s96, 192
	s_movk_i32 s2, 64
	s_mov_b32 s98, 3
	s_mov_b32 s100, 5
	s_mov_b32 s99, 1
	v_readlane_b32 s6, v239, 34
	v_readlane_b32 s7, v239, 35
	s_nop 3
	s_sub_u32 s6, s6, 0x128
	s_subb_u32 s7, s7, 0
	s_load_dwordx2 s[82:83], s[6:7], 0xc8
	s_waitcnt lgkmcnt(0)
	s_branch .Lconv_entry
.Lconv_ret_h0:
	s_mov_b32 s99, 0
	s_add_i32 s96, s96, 192
	s_mov_b32 s2, s101
	s_add_u32 s82, s58, 0x32100000
	s_addc_u32 s83, s59, 0
	s_mov_b64 exec, -1
	s_mov_b64 s[0:1], -1
	s_branch .LBB0_417
